# MoE up: GEMM workgroup count chosen from the routed tile count (238 only when nT=68)
# speedup vs baseline: 1.0092x; 1.0007x over previous
;     int tid = threadIdx.x; asm volatile("" : "+v"(tid)); const int lane = tid & 63, wave = __builtin_amdgcn_readfirstlane(tid >> 6);
;     unsigned nxt = CQ_END; int left = quota;
; __global__ void __launch_bounds__(NWAVES * 64, 2) trunk_fwd(Args args) {
;     ...
;             else { const int nT = __builtin_amdgcn_readfirstlane(TILEE[127]);
;                 const int gg = (G == 256) ? 238 : G;
;                 if (bx < gg) { pg8::Gemm g{HPERM, MUP_T, nT * 256, 2 * FFE, D, (size_t)2 * FFE * D * 2}; pg8::MoeOrder S; S.init(nT, 2 * FFE, gg, bx, TILEE); pg8::EpiSwiglu E{GBUF, FFE / 2, 28, (size_t)MAXPT * 256 * (FFE / 2)};
;                     pg8::gemm_phase(lds, g, S, E, tz, ctl + CW_DONE(10)); }
;                 else conv_run(args.in[I_M1], args.in[I_M3], args.in[I_M2], MUP_T, MDN_T, ctl, MISC + 16, true, ctl + CW_DONE(10), 16u, 1 << 30, 1);
.LBB0_1053:
	s_andn2_b64 vcc, exec, s[0:1]
	s_cbranch_vccnz .LBB0_1245
	v_readlane_b32 s4, v255, 19
	v_readlane_b32 s5, v255, 20
	v_mov_b32_e32 v1, v0
	s_mov_b64 s[0:1], -1
	s_and_b64 vcc, exec, s[4:5]
	s_cbranch_vccz .LBB0_1140
	v_readlane_b32 s0, v252, 27
	v_readlane_b32 s1, v252, 28
	v_readlane_b32 s4, v252, 37
	s_nop 3
	global_load_dword v2, v187, s[0:1]
	s_waitcnt vmcnt(0)
	v_readfirstlane_b32 s28, v2
	s_cmpk_lg_i32 s33, 0x100
	s_cbranch_scc1 .Lmoe_gg_done
	s_mul_i32 s5, s28, 56
	s_add_i32 s0, s5, 0xf9
	s_mul_hi_u32 s0, s0, 0x10624de
	s_movk_i32 s4, 0xe0
.Lmoe_gg_loop:
	s_mul_i32 s1, s4, s0
	s_cmp_ge_u32 s1, s5
	s_cbranch_scc1 .Lmoe_gg_done
	s_add_i32 s4, s4, 1
	s_cmpk_lt_u32 s4, 0xfa
	s_cbranch_scc1 .Lmoe_gg_loop
.Lmoe_gg_done:
	v_writelane_b32 v252, s4, 37
	v_readlane_b32 s5, v254, 40
	s_mov_b64 s[0:1], -1
	s_cmp_ge_i32 s5, s4
	s_cselect_b64 s[4:5], -1, 0
	s_and_b64 vcc, exec, s[4:5]
	s_cbranch_vccz .LBB0_1087
	v_mov_b32_e32 v2, v0
	v_mov_b32_e32 v127, 2.0
	v_readfirstlane_b32 s12, v2
	v_cmp_eq_u32_e64 s[0:1], 0, v2
	v_mov_b32_e32 v129, -1
	s_and_saveexec_b64 s[4:5], s[0:1]
	s_cbranch_execz .LBB0_1064
	v_readlane_b32 s8, v252, 35
	v_readlane_b32 s9, v252, 36
	s_mov_b64 s[6:7], exec
	v_mbcnt_lo_u32_b32 v4, s6, 0
	v_mbcnt_hi_u32_b32 v4, s7, v4
	v_cmp_eq_u32_e32 vcc, 0, v4
	s_nop 0
	global_load_dword v3, v187, s[8:9] sc1
	s_and_saveexec_b64 s[8:9], vcc
	s_cbranch_execz .LBB0_1059
	s_bcnt1_i32_b64 s6, s[6:7]
	v_mov_b32_e32 v5, s6
	v_readlane_b32 s6, v250, 18
	v_readlane_b32 s7, v250, 19
	s_nop 4
	global_atomic_add v5, v187, v5, s[6:7] sc0
